# speedup vs baseline: 1.0043x; 1.0017x over previous
amdhsa.kernels:
  - .agpr_count:     0
    .args:
      - .offset:         0
        .size:           144
        .value_kind:     by_value
    .group_segment_fixed_size: 16640
    .kernarg_segment_align: 8
    .kernarg_segment_size: 144
    .language:       OpenCL C
    .language_version:
      - 2
      - 0
    .max_flat_workgroup_size: 256
    .name:           _Z8prep_ln18PrepArgs
    .private_segment_fixed_size: 0
    .sgpr_count:     22
    .sgpr_spill_count: 0
    .symbol:         _Z8prep_ln18PrepArgs.kd
    .uniform_work_group_size: 1
    .uses_dynamic_stack: false
    .vgpr_count:     63
    .vgpr_spill_count: 0
    .wavefront_size: 64
  - .agpr_count:     0
    .args:
      - .address_space:  global
        .offset:         0
        .size:           8
        .value_kind:     global_buffer
      - .address_space:  global
        .offset:         8
        .size:           8
        .value_kind:     global_buffer
      - .address_space:  global
        .offset:         16
        .size:           8
        .value_kind:     global_buffer
      - .address_space:  global
        .offset:         24
        .size:           8
        .value_kind:     global_buffer
      - .offset:         32
        .size:           144
        .value_kind:     by_value
    .group_segment_fixed_size: 0
    .kernarg_segment_align: 8
    .kernarg_segment_size: 176
    .language:       OpenCL C
    .language_version:
      - 2
      - 0
    .max_flat_workgroup_size: 256
    .name:           _Z10attn64_fwdPKtS0_S0_Pt8PrepArgs
    .private_segment_fixed_size: 0
    .sgpr_count:     66
    .sgpr_spill_count: 0
    .symbol:         _Z10attn64_fwdPKtS0_S0_Pt8PrepArgs.kd
    .uniform_work_group_size: 1
    .uses_dynamic_stack: false
    .vgpr_count:     223
    .vgpr_spill_count: 0
    .wavefront_size: 64
  - .agpr_count:     0
    .args:
      - .address_space:  global
        .offset:         0
        .size:           8
        .value_kind:     global_buffer
      - .address_space:  global
        .offset:         8
        .size:           8
        .value_kind:     global_buffer
      - .offset:         16
        .size:           4
        .value_kind:     by_value
      - .offset:         20
        .size:           4
        .value_kind:     by_value
      - .offset:         24
        .size:           64
        .value_kind:     by_value
    .group_segment_fixed_size: 0
    .kernarg_segment_align: 8
    .kernarg_segment_size: 88
    .language:       OpenCL C
    .language_version:
      - 2
      - 0
    .max_flat_workgroup_size: 256
    .name:           _Z8gemm2b_kILi2EEvPKtS1_ii7EpiArgs
    .private_segment_fixed_size: 0
    .sgpr_count:     98
    .sgpr_spill_count: 0
    .symbol:         _Z8gemm2b_kILi2EEvPKtS1_ii7EpiArgs.kd
    .uniform_work_group_size: 1
    .uses_dynamic_stack: false
    .vgpr_count:     212
    .vgpr_spill_count: 0
    .wavefront_size: 64
  - .agpr_count:     0
    .args:
      - .address_space:  global
        .offset:         0
        .size:           8
        .value_kind:     global_buffer
      - .address_space:  global
        .offset:         8
        .size:           8
        .value_kind:     global_buffer
      - .offset:         16
        .size:           4
        .value_kind:     by_value
      - .offset:         20
        .size:           4
        .value_kind:     by_value
      - .offset:         24
        .size:           64
        .value_kind:     by_value
    .group_segment_fixed_size: 0
    .kernarg_segment_align: 8
    .kernarg_segment_size: 88
    .language:       OpenCL C
    .language_version:
      - 2
      - 0
    .max_flat_workgroup_size: 256
    .name:           _Z8gemm2b_kILi0EEvPKtS1_ii7EpiArgs
    .private_segment_fixed_size: 0
    .sgpr_count:     85
    .sgpr_spill_count: 0
    .symbol:         _Z8gemm2b_kILi0EEvPKtS1_ii7EpiArgs.kd
    .uniform_work_group_size: 1
    .uses_dynamic_stack: false
    .vgpr_count:     186
    .vgpr_spill_count: 0
    .wavefront_size: 64
  - .agpr_count:     0
    .args:
      - .address_space:  global
        .offset:         0
        .size:           8
        .value_kind:     global_buffer
      - .address_space:  global
        .offset:         8
        .size:           8
        .value_kind:     global_buffer
      - .offset:         16
        .size:           4
        .value_kind:     by_value
      - .offset:         20
        .size:           4
        .value_kind:     by_value
      - .offset:         24
        .size:           64
        .value_kind:     by_value
    .group_segment_fixed_size: 0
    .kernarg_segment_align: 8
    .kernarg_segment_size: 88
    .language:       OpenCL C
    .language_version:
      - 2
      - 0
    .max_flat_workgroup_size: 512
    .name:           _Z6gemm_kILi1ELb1ELb0ELb1ELb1ELb0EEvPKtS1_ii7EpiArgs
    .private_segment_fixed_size: 0
    .sgpr_count:     61
    .sgpr_spill_count: 0
    .symbol:         _Z6gemm_kILi1ELb1ELb0ELb1ELb1ELb0EEvPKtS1_ii7EpiArgs.kd
    .uniform_work_group_size: 1
    .uses_dynamic_stack: false
    .vgpr_count:     116
    .vgpr_spill_count: 0
    .wavefront_size: 64
  - .agpr_count:     0
    .args:
      - .address_space:  global
        .offset:         0
        .size:           8
        .value_kind:     global_buffer
      - .address_space:  global
        .offset:         8
        .size:           8
        .value_kind:     global_buffer
      - .offset:         16
        .size:           4
        .value_kind:     by_value
      - .offset:         20
        .size:           4
        .value_kind:     by_value
      - .offset:         24
        .size:           64
        .value_kind:     by_value
    .group_segment_fixed_size: 0
    .kernarg_segment_align: 8
    .kernarg_segment_size: 88
    .language:       OpenCL C
    .language_version:
      - 2
      - 0
    .max_flat_workgroup_size: 512
    .name:           _Z6gemm_kILi1ELb1ELb1ELb0ELb0ELb1EEvPKtS1_ii7EpiArgs
    .private_segment_fixed_size: 0
    .sgpr_count:     84
    .sgpr_spill_count: 0
    .symbol:         _Z6gemm_kILi1ELb1ELb1ELb0ELb0ELb1EEvPKtS1_ii7EpiArgs.kd
    .uniform_work_group_size: 1
    .uses_dynamic_stack: false
    .vgpr_count:     224
    .vgpr_spill_count: 0
    .wavefront_size: 64
